# static s_setprio 1 for waves 4-7 during the PEER E1/E2 matrix-core streams (reset at phase exit)
# speedup vs baseline: 1.0078x; 1.0066x over previous
.Le1w_first:
	v_readfirstlane_b32 s98, v0
	s_nop 3
	s_cmp_ge_u32 s98, 0x100
	s_cbranch_scc0 .Lpr_e1
	s_setprio 1

.LBB0_735:
	s_setprio 0
	s_waitcnt vmcnt(0)
	s_barrier
	s_and_saveexec_b64 s[0:1], s[44:45]
	v_readlane_b32 s56, v255, 27
	v_readlane_b32 s76, v255, 50
	v_readlane_b32 s26, v255, 54
	v_readlane_b32 s57, v255, 28
	s_mov_b32 s27, 0xbfb8aa3b
	s_mov_b32 s33, 0x378e98ab
	s_mov_b32 s58, 0x3b7cd369
	s_mov_b32 s59, 0xbcc618b2
	s_mov_b32 s61, 0x3dda74e4
	s_mov_b32 s62, 0x3f228afd
	s_mov_b32 s63, 0x3e03c728
	s_mov_b32 s6, 0x42ce8ed0
	s_mov_b32 s7, 0xc2b17218
	s_brev_b32 s38, -2
	v_readlane_b32 s77, v255, 51
	s_cbranch_execz .LBB0_783
	v_readlane_b32 s2, v255, 29
	s_waitcnt vmcnt(0) expcnt(0) lgkmcnt(0)
	s_nop 0
	v_mov_b32_e32 v2, s2
	ds_read_b32 v4, v2
	v_readlane_b32 s2, v255, 30
	s_waitcnt lgkmcnt(0)
	v_cmp_ne_u32_e32 vcc, 0, v4
	v_mov_b32_e32 v2, s2
	ds_read_b32 v2, v2
	s_cbranch_vccnz .LBB0_751
	v_readlane_b32 s4, v253, 16
	v_readlane_b32 s5, v253, 17
	s_load_dwordx2 s[2:3], s[4:5], 0x4
	s_waitcnt lgkmcnt(0)
	s_mul_i32 s2, s2, s86
	s_mul_i32 s2, s2, s3
	s_mov_b32 s3, 1
	s_branch .LBB0_739

.LBB0_899:
	s_setprio 0
	s_mov_b64 s[0:1], -1
	v_writelane_b32 v255, s0, 31
	s_andn2_b64 vcc, exec, s[30:31]
	s_movk_i32 s58, 0x2c00
	v_writelane_b32 v255, s1, 32
	s_mov_b64 s[0:1], -1
	v_readlane_b32 s60, v255, 45
	v_readlane_b32 s61, v255, 46
	s_cbranch_vccz .LBB0_900
	s_getpc_b64 s[98:99]
